# down GEMM epilogue: s_waitcnt vmcnt(0) ahead of the prefetched-bias use counted down to vmcnt(10) (the guarded loads retire before the K-loop ends; 0 drained the next unit's staged tiles) + previous (
# speedup vs baseline: 1.0102x; 1.0102x over previous
.LBB0_1627:
	v_lshlrev_b32_e32 v158, 16, v6
	v_and_b32_e32 v159, 0xffff0000, v6
	v_lshlrev_b32_e32 v154, 16, v8
	v_and_b32_e32 v155, 0xffff0000, v8
	v_lshlrev_b32_e32 v156, 16, v7
	v_and_b32_e32 v157, 0xffff0000, v7
	v_lshlrev_b32_e32 v152, 16, v9
	v_and_b32_e32 v153, 0xffff0000, v9
	s_waitcnt vmcnt(10)
	v_lshlrev_b32_e32 v6, 16, v4
	v_and_b32_e32 v7, 0xffff0000, v4
	v_mul_f32_e32 v4, 0x41000000, v146
	v_pk_fma_f32 v[134:135], v[134:135], s[36:37], v[158:159] op_sel_hi:[1,0,1]
	v_pk_fma_f32 v[130:131], v[130:131], s[36:37], v[154:155] op_sel_hi:[1,0,1]
	v_pk_fma_f32 v[136:137], v[136:137], s[36:37], v[156:157] op_sel_hi:[1,0,1]
	v_pk_mul_f32 v[134:135], v[4:5], v[134:135] op_sel_hi:[0,1]
	v_pk_fma_f32 v[132:133], v[132:133], s[36:37], v[152:153] op_sel_hi:[1,0,1]
	v_pk_mul_f32 v[130:131], v[4:5], v[130:131] op_sel_hi:[0,1]
	v_lshlrev_b32_e32 v150, 16, v2
	v_and_b32_e32 v151, 0xffff0000, v2
	v_lshlrev_b32_e32 v8, 16, v3
	v_and_b32_e32 v9, 0xffff0000, v3
	v_lshlrev_b32_e32 v2, 16, v5
	v_and_b32_e32 v3, 0xffff0000, v5
	v_pk_mul_f32 v[136:137], v[4:5], v[136:137] op_sel_hi:[0,1]
	v_pk_mul_f32 v[132:133], v[4:5], v[132:133] op_sel_hi:[0,1]
	v_med3_f32 v5, v134, s70, v164
	v_med3_f32 v134, v130, s70, v164
	v_med3_f32 v135, v135, s70, v164
	v_mov_b32_e32 v130, 0
	v_cvt_pk_fp8_f32 v130, v5, v135
	v_med3_f32 v136, v136, s70, v164
	v_med3_f32 v5, v137, s70, v164
	v_pk_fma_f32 v[126:127], v[126:127], s[36:37], v[150:151] op_sel_hi:[1,0,1]
	v_pk_fma_f32 v[128:129], v[128:129], s[36:37], v[8:9] op_sel_hi:[1,0,1]
	v_pk_fma_f32 v[122:123], v[122:123], s[36:37], v[6:7] op_sel_hi:[1,0,1]
	v_pk_fma_f32 v[124:125], v[124:125], s[36:37], v[2:3] op_sel_hi:[1,0,1]
	v_cvt_pk_fp8_f32 v130, v136, v5 op_sel:[0,0,1]
	v_pk_mul_f32 v[128:129], v[4:5], v[128:129] op_sel_hi:[0,1]
	v_pk_mul_f32 v[126:127], v[4:5], v[126:127] op_sel_hi:[0,1]
	v_pk_mul_f32 v[124:125], v[4:5], v[124:125] op_sel_hi:[0,1]
	v_pk_mul_f32 v[4:5], v[4:5], v[122:123] op_sel_hi:[0,1]
	v_med3_f32 v146, v131, s70, v164
	v_mov_b32_e32 v131, 0
	v_med3_f32 v122, v126, s70, v164
	v_med3_f32 v123, v4, s70, v164
	v_med3_f32 v126, v127, s70, v164
	v_med3_f32 v127, v5, s70, v164
	v_mov_b32_e32 v4, 0
	v_mov_b32_e32 v5, 0
	v_cvt_pk_fp8_f32 v131, v134, v146
	v_cvt_pk_fp8_f32 v4, v122, v126
	v_cvt_pk_fp8_f32 v5, v123, v127
	v_mov_b32_e32 v171, v0
	v_med3_f32 v132, v132, s70, v164
	v_readfirstlane_b32 s39, v171
	s_lshr_b32 s6, s39, 6
	v_med3_f32 v133, v133, s70, v164
	v_med3_f32 v128, v128, s70, v164
	v_med3_f32 v124, v124, s70, v164
	v_med3_f32 v122, v129, s70, v164
	v_med3_f32 v123, v125, s70, v164
	s_mulk_i32 s6, 0xb00
	v_cvt_pk_fp8_f32 v131, v132, v133 op_sel:[0,0,1]
	v_cvt_pk_fp8_f32 v4, v128, v122 op_sel:[0,0,1]
	v_cvt_pk_fp8_f32 v5, v124, v123 op_sel:[0,0,1]
	s_add_i32 s6, s6, 0
	v_and_b32_e32 v172, 15, v171
	v_lshrrev_b32_e32 v123, 1, v171
	s_add_i32 s41, s6, 0x20000
	v_mul_u32_u24_e32 v122, 0x50, v172
	v_and_b32_e32 v123, 24, v123
	v_add3_u32 v122, s41, v122, v123
	s_and_b32 s7, s39, 0xc0
	ds_write2_b64 v122, v[130:131], v[4:5] offset1:4
	v_bfe_u32 v4, v171, 2, 4
	s_ashr_i32 s39, s39, 2
	v_mul_u32_u24_e32 v5, 0x50, v4
	v_lshlrev_b32_e32 v123, 4, v171
	s_andn2_b32 s39, s39, 63
	v_lshl_or_b32 v4, s48, 8, v4
	v_and_b32_e32 v146, 48, v123
	v_add_u32_e32 v4, s39, v4
	v_mul_f32_e32 v130, 0x41000000, v170
	v_pk_fma_f32 v[118:119], v[118:119], s[36:37], v[158:159] op_sel_hi:[1,0,1]
	v_pk_fma_f32 v[114:115], v[114:115], s[36:37], v[154:155] op_sel_hi:[1,0,1]
	v_add3_u32 v123, s41, v5, v146
	v_ashrrev_i32_e32 v5, 31, v4
	v_pk_mul_f32 v[118:119], v[130:131], v[118:119] op_sel_hi:[0,1]
	v_pk_mul_f32 v[114:115], v[130:131], v[114:115] op_sel_hi:[0,1]
	v_lshlrev_b64 v[128:129], 10, v[4:5]
	v_med3_f32 v5, v118, s70, v164
	v_med3_f32 v118, v114, s70, v164
	v_med3_f32 v119, v119, s70, v164
	v_mov_b32_e32 v114, v147
	v_cvt_pk_fp8_f32 v114, v5, v119
	v_pk_fma_f32 v[120:121], v[120:121], s[36:37], v[156:157] op_sel_hi:[1,0,1]
	v_pk_fma_f32 v[116:117], v[116:117], s[36:37], v[152:153] op_sel_hi:[1,0,1]
	v_pk_mul_f32 v[120:121], v[130:131], v[120:121] op_sel_hi:[0,1]
	v_pk_mul_f32 v[116:117], v[130:131], v[116:117] op_sel_hi:[0,1]
	v_med3_f32 v131, v115, s70, v164
	v_pk_fma_f32 v[110:111], v[110:111], s[36:37], v[150:151] op_sel_hi:[1,0,1]
	v_pk_fma_f32 v[106:107], v[106:107], s[36:37], v[6:7] op_sel_hi:[1,0,1]
	v_med3_f32 v120, v120, s70, v164
	v_med3_f32 v5, v121, s70, v164
	v_pk_mul_f32 v[110:111], v[130:131], v[110:111] op_sel_hi:[0,1]
	v_pk_mul_f32 v[106:107], v[130:131], v[106:107] op_sel_hi:[0,1]
	v_cvt_pk_fp8_f32 v114, v120, v5 op_sel:[0,0,1]
	v_med3_f32 v5, v110, s70, v164
	v_med3_f32 v110, v106, s70, v164
	v_med3_f32 v111, v111, s70, v164
	v_mov_b32_e32 v106, v147
	v_cvt_pk_fp8_f32 v106, v5, v111
	v_pk_fma_f32 v[112:113], v[112:113], s[36:37], v[8:9] op_sel_hi:[1,0,1]
	v_mov_b32_e32 v115, v147
	v_pk_mul_f32 v[112:113], v[130:131], v[112:113] op_sel_hi:[0,1]
	v_med3_f32 v112, v112, s70, v164
	v_med3_f32 v5, v113, s70, v164
	v_cvt_pk_fp8_f32 v106, v112, v5 op_sel:[0,0,1]
	v_mul_f32_e32 v112, 0x41000000, v169
	v_pk_fma_f32 v[102:103], v[102:103], s[36:37], v[158:159] op_sel_hi:[1,0,1]
	v_pk_fma_f32 v[98:99], v[98:99], s[36:37], v[154:155] op_sel_hi:[1,0,1]
	v_cvt_pk_fp8_f32 v115, v118, v131
	v_pk_mul_f32 v[102:103], v[112:113], v[102:103] op_sel_hi:[0,1]
	v_pk_mul_f32 v[98:99], v[112:113], v[98:99] op_sel_hi:[0,1]
	v_med3_f32 v5, v102, s70, v164
	v_med3_f32 v102, v98, s70, v164
	v_med3_f32 v103, v103, s70, v164
	v_mov_b32_e32 v98, v147
	v_cvt_pk_fp8_f32 v98, v5, v103
	v_med3_f32 v116, v116, s70, v164
	v_med3_f32 v117, v117, s70, v164
	v_pk_fma_f32 v[104:105], v[104:105], s[36:37], v[156:157] op_sel_hi:[1,0,1]
	v_pk_fma_f32 v[100:101], v[100:101], s[36:37], v[152:153] op_sel_hi:[1,0,1]
	v_cvt_pk_fp8_f32 v115, v116, v117 op_sel:[0,0,1]
	v_med3_f32 v116, v107, s70, v164
	v_mov_b32_e32 v107, v147
	v_pk_mul_f32 v[104:105], v[112:113], v[104:105] op_sel_hi:[0,1]
	v_pk_mul_f32 v[100:101], v[112:113], v[100:101] op_sel_hi:[0,1]
	v_med3_f32 v113, v99, s70, v164
	v_pk_fma_f32 v[94:95], v[94:95], s[36:37], v[150:151] op_sel_hi:[1,0,1]
	v_pk_fma_f32 v[90:91], v[90:91], s[36:37], v[6:7] op_sel_hi:[1,0,1]
	v_cvt_pk_fp8_f32 v107, v110, v116
	v_med3_f32 v104, v104, s70, v164
	v_med3_f32 v5, v105, s70, v164
	v_pk_mul_f32 v[94:95], v[112:113], v[94:95] op_sel_hi:[0,1]
	v_pk_mul_f32 v[90:91], v[112:113], v[90:91] op_sel_hi:[0,1]
	v_pk_fma_f32 v[108:109], v[108:109], s[36:37], v[2:3] op_sel_hi:[1,0,1]
	v_mov_b32_e32 v99, v147
	v_cvt_pk_fp8_f32 v98, v104, v5 op_sel:[0,0,1]
	v_med3_f32 v5, v94, s70, v164
	v_med3_f32 v94, v90, s70, v164
	v_med3_f32 v95, v95, s70, v164
	v_mov_b32_e32 v90, v147
	s_lshl_b32 s6, s50, 8
	ds_read_b128 v[124:127], v123
	v_pk_mul_f32 v[108:109], v[130:131], v[108:109] op_sel_hi:[0,1]
	v_cvt_pk_fp8_f32 v99, v102, v113
	v_cvt_pk_fp8_f32 v90, v5, v95
	s_or_b32 s6, s7, s6
	v_med3_f32 v108, v108, s70, v164
	v_med3_f32 v109, v109, s70, v164
	v_pk_fma_f32 v[96:97], v[96:97], s[36:37], v[8:9] op_sel_hi:[1,0,1]
	s_ashr_i32 s7, s6, 31
	v_lshl_add_u64 v[128:129], s[16:17], 0, v[128:129]
	v_cvt_pk_fp8_f32 v107, v108, v109 op_sel:[0,0,1]
	v_pk_mul_f32 v[96:97], v[112:113], v[96:97] op_sel_hi:[0,1]
	v_lshl_add_u64 v[128:129], v[128:129], 0, s[6:7]
	v_med3_f32 v100, v100, s70, v164
	v_med3_f32 v101, v101, s70, v164
	v_med3_f32 v96, v96, s70, v164
	v_med3_f32 v5, v97, s70, v164
	v_lshl_add_u64 v[108:109], v[128:129], 0, v[146:147]
	v_cvt_pk_fp8_f32 v99, v100, v101 op_sel:[0,0,1]
	v_med3_f32 v100, v91, s70, v164
	v_mov_b32_e32 v91, v147
	v_cvt_pk_fp8_f32 v90, v96, v5 op_sel:[0,0,1]
	v_mul_f32_e32 v96, 0x41000000, v168
	v_pk_fma_f32 v[78:79], v[78:79], s[36:37], v[158:159] op_sel_hi:[1,0,1]
	v_pk_fma_f32 v[74:75], v[74:75], s[36:37], v[154:155] op_sel_hi:[1,0,1]
	s_waitcnt lgkmcnt(0)
	global_store_dwordx4 v[108:109], v[124:127], off
	v_cvt_pk_fp8_f32 v91, v94, v100
	v_pk_fma_f32 v[80:81], v[80:81], s[36:37], v[156:157] op_sel_hi:[1,0,1]
	v_pk_mul_f32 v[78:79], v[96:97], v[78:79] op_sel_hi:[0,1]
	v_pk_fma_f32 v[76:77], v[76:77], s[36:37], v[152:153] op_sel_hi:[1,0,1]
	v_pk_mul_f32 v[74:75], v[96:97], v[74:75] op_sel_hi:[0,1]
	ds_write2_b64 v122, v[114:115], v[106:107] offset1:4
	v_or_b32_e32 v110, 16, v4
	v_pk_fma_f32 v[92:93], v[92:93], s[36:37], v[2:3] op_sel_hi:[1,0,1]
	v_pk_mul_f32 v[80:81], v[96:97], v[80:81] op_sel_hi:[0,1]
	v_pk_mul_f32 v[76:77], v[96:97], v[76:77] op_sel_hi:[0,1]
	v_med3_f32 v5, v78, s70, v164
	v_med3_f32 v78, v74, s70, v164
	v_med3_f32 v79, v79, s70, v164
	v_med3_f32 v97, v75, s70, v164
	v_mov_b32_e32 v74, v147
	v_mov_b32_e32 v75, v147
	ds_read_b128 v[106:109], v123
	v_ashrrev_i32_e32 v111, 31, v110
	v_pk_mul_f32 v[92:93], v[112:113], v[92:93] op_sel_hi:[0,1]
	v_cvt_pk_fp8_f32 v74, v5, v79
	v_cvt_pk_fp8_f32 v75, v78, v97
	v_lshlrev_b64 v[110:111], 10, v[110:111]
	v_med3_f32 v92, v92, s70, v164
	v_med3_f32 v93, v93, s70, v164
	v_lshl_add_u64 v[110:111], s[16:17], 0, v[110:111]
	v_cvt_pk_fp8_f32 v91, v92, v93 op_sel:[0,0,1]
	v_pk_fma_f32 v[62:63], v[62:63], s[36:37], v[150:151] op_sel_hi:[1,0,1]
	v_pk_fma_f32 v[58:59], v[58:59], s[36:37], v[6:7] op_sel_hi:[1,0,1]
	v_lshl_add_u64 v[110:111], v[110:111], 0, s[6:7]
	v_med3_f32 v80, v80, s70, v164
	v_med3_f32 v76, v76, s70, v164
	v_med3_f32 v5, v81, s70, v164
	v_med3_f32 v77, v77, s70, v164
	v_pk_mul_f32 v[62:63], v[96:97], v[62:63] op_sel_hi:[0,1]
	v_pk_mul_f32 v[58:59], v[96:97], v[58:59] op_sel_hi:[0,1]
	v_lshl_add_u64 v[92:93], v[110:111], 0, v[146:147]
	v_cvt_pk_fp8_f32 v74, v80, v5 op_sel:[0,0,1]
	v_cvt_pk_fp8_f32 v75, v76, v77 op_sel:[0,0,1]
	v_med3_f32 v5, v62, s70, v164
	v_med3_f32 v62, v58, s70, v164
	v_med3_f32 v63, v63, s70, v164
	v_med3_f32 v76, v59, s70, v164
	v_mov_b32_e32 v58, v147
	v_mov_b32_e32 v59, v147
	s_waitcnt lgkmcnt(0)
	global_store_dwordx4 v[92:93], v[106:109], off
	v_cvt_pk_fp8_f32 v58, v5, v63
	v_cvt_pk_fp8_f32 v59, v62, v76
	ds_write2_b64 v122, v[98:99], v[90:91] offset1:4
	v_or_b32_e32 v94, 32, v4
	v_pk_fma_f32 v[64:65], v[64:65], s[36:37], v[8:9] op_sel_hi:[1,0,1]
	v_pk_fma_f32 v[60:61], v[60:61], s[36:37], v[2:3] op_sel_hi:[1,0,1]
	ds_read_b128 v[90:93], v123
	v_ashrrev_i32_e32 v95, 31, v94
	v_pk_mul_f32 v[64:65], v[96:97], v[64:65] op_sel_hi:[0,1]
	v_pk_mul_f32 v[60:61], v[96:97], v[60:61] op_sel_hi:[0,1]
	v_lshlrev_b64 v[94:95], 10, v[94:95]
	v_med3_f32 v64, v64, s70, v164
	v_med3_f32 v60, v60, s70, v164
	v_med3_f32 v5, v65, s70, v164
	v_med3_f32 v61, v61, s70, v164
	v_lshl_add_u64 v[94:95], s[16:17], 0, v[94:95]
	v_cvt_pk_fp8_f32 v58, v64, v5 op_sel:[0,0,1]
	v_cvt_pk_fp8_f32 v59, v60, v61 op_sel:[0,0,1]
	v_lshl_add_u64 v[94:95], v[94:95], 0, s[6:7]
	v_lshl_add_u64 v[60:61], v[94:95], 0, v[146:147]
	s_waitcnt lgkmcnt(0)
	global_store_dwordx4 v[60:61], v[90:93], off
	ds_write2_b64 v122, v[74:75], v[58:59] offset1:4
	v_mul_f32_e32 v64, 0x41000000, v167
	v_pk_fma_f32 v[74:75], v[86:87], s[36:37], v[158:159] op_sel_hi:[1,0,1]
	v_pk_fma_f32 v[78:79], v[82:83], s[36:37], v[154:155] op_sel_hi:[1,0,1]
	v_pk_mul_f32 v[74:75], v[64:65], v[74:75] op_sel_hi:[0,1]
	v_pk_fma_f32 v[76:77], v[88:89], s[36:37], v[156:157] op_sel_hi:[1,0,1]
	v_pk_fma_f32 v[80:81], v[84:85], s[36:37], v[152:153] op_sel_hi:[1,0,1]
	v_pk_mul_f32 v[78:79], v[64:65], v[78:79] op_sel_hi:[0,1]
	v_med3_f32 v5, v74, s70, v164
	v_med3_f32 v75, v75, s70, v164
	v_mov_b32_e32 v74, v147
	v_pk_mul_f32 v[76:77], v[64:65], v[76:77] op_sel_hi:[0,1]
	v_pk_mul_f32 v[80:81], v[64:65], v[80:81] op_sel_hi:[0,1]
	v_med3_f32 v65, v78, s70, v164
	v_med3_f32 v78, v79, s70, v164
	v_cvt_pk_fp8_f32 v74, v5, v75
	v_mov_b32_e32 v75, v147
	v_cvt_pk_fp8_f32 v75, v65, v78
	v_med3_f32 v79, v80, s70, v164
	v_med3_f32 v65, v81, s70, v164
	v_pk_fma_f32 v[70:71], v[70:71], s[36:37], v[150:151] op_sel_hi:[1,0,1]
	v_pk_fma_f32 v[72:73], v[72:73], s[36:37], v[8:9] op_sel_hi:[1,0,1]
	v_pk_fma_f32 v[66:67], v[66:67], s[36:37], v[6:7] op_sel_hi:[1,0,1]
	v_pk_fma_f32 v[68:69], v[68:69], s[36:37], v[2:3] op_sel_hi:[1,0,1]
	v_med3_f32 v76, v76, s70, v164
	v_med3_f32 v5, v77, s70, v164
	v_cvt_pk_fp8_f32 v75, v79, v65 op_sel:[0,0,1]
	v_pk_mul_f32 v[72:73], v[64:65], v[72:73] op_sel_hi:[0,1]
	v_pk_mul_f32 v[70:71], v[64:65], v[70:71] op_sel_hi:[0,1]
	v_pk_mul_f32 v[68:69], v[64:65], v[68:69] op_sel_hi:[0,1]
	v_pk_mul_f32 v[64:65], v[64:65], v[66:67] op_sel_hi:[0,1]
	v_cvt_pk_fp8_f32 v74, v76, v5 op_sel:[0,0,1]
	v_med3_f32 v5, v70, s70, v164
	v_med3_f32 v66, v64, s70, v164
	v_med3_f32 v67, v71, s70, v164
	v_med3_f32 v70, v65, s70, v164
	v_mov_b32_e32 v64, v147
	v_mov_b32_e32 v65, v147
	v_cvt_pk_fp8_f32 v64, v5, v67
	v_cvt_pk_fp8_f32 v65, v66, v70
	v_or_b32_e32 v62, 48, v4
	ds_read_b128 v[58:61], v123
	v_ashrrev_i32_e32 v63, 31, v62
	v_lshlrev_b64 v[62:63], 10, v[62:63]
	v_med3_f32 v71, v72, s70, v164
	v_med3_f32 v68, v68, s70, v164
	v_med3_f32 v5, v73, s70, v164
	v_med3_f32 v66, v69, s70, v164
	v_lshl_add_u64 v[62:63], s[16:17], 0, v[62:63]
	v_cvt_pk_fp8_f32 v64, v71, v5 op_sel:[0,0,1]
	v_cvt_pk_fp8_f32 v65, v68, v66 op_sel:[0,0,1]
	v_lshl_add_u64 v[62:63], v[62:63], 0, s[6:7]
	v_lshl_add_u64 v[62:63], v[62:63], 0, v[146:147]
	s_waitcnt lgkmcnt(0)
	global_store_dwordx4 v[62:63], v[58:61], off
	ds_write2_b64 v122, v[74:75], v[64:65] offset1:4
	v_mul_f32_e32 v64, 0x41000000, v166
	v_pk_fma_f32 v[54:55], v[54:55], s[36:37], v[158:159] op_sel_hi:[1,0,1]
	v_pk_fma_f32 v[50:51], v[50:51], s[36:37], v[154:155] op_sel_hi:[1,0,1]
	v_pk_mul_f32 v[54:55], v[64:65], v[54:55] op_sel_hi:[0,1]
	v_pk_mul_f32 v[50:51], v[64:65], v[50:51] op_sel_hi:[0,1]
	v_med3_f32 v5, v54, s70, v164
	v_med3_f32 v54, v50, s70, v164
	v_med3_f32 v55, v55, s70, v164
	v_mov_b32_e32 v50, v147
	v_cvt_pk_fp8_f32 v50, v5, v55
	v_pk_fma_f32 v[56:57], v[56:57], s[36:37], v[156:157] op_sel_hi:[1,0,1]
	v_pk_fma_f32 v[52:53], v[52:53], s[36:37], v[152:153] op_sel_hi:[1,0,1]
	v_pk_mul_f32 v[56:57], v[64:65], v[56:57] op_sel_hi:[0,1]
	v_pk_mul_f32 v[52:53], v[64:65], v[52:53] op_sel_hi:[0,1]
	v_med3_f32 v65, v51, s70, v164
	v_pk_fma_f32 v[46:47], v[46:47], s[36:37], v[150:151] op_sel_hi:[1,0,1]
	v_pk_fma_f32 v[42:43], v[42:43], s[36:37], v[6:7] op_sel_hi:[1,0,1]
	v_med3_f32 v56, v56, s70, v164
	v_med3_f32 v5, v57, s70, v164
	v_pk_mul_f32 v[46:47], v[64:65], v[46:47] op_sel_hi:[0,1]
	v_pk_mul_f32 v[42:43], v[64:65], v[42:43] op_sel_hi:[0,1]
	v_cvt_pk_fp8_f32 v50, v56, v5 op_sel:[0,0,1]
	v_med3_f32 v5, v46, s70, v164
	v_med3_f32 v46, v42, s70, v164
	v_med3_f32 v47, v47, s70, v164
	v_mov_b32_e32 v42, v147
	v_cvt_pk_fp8_f32 v42, v5, v47
	v_pk_fma_f32 v[48:49], v[48:49], s[36:37], v[8:9] op_sel_hi:[1,0,1]
	v_mov_b32_e32 v51, v147
	v_pk_mul_f32 v[48:49], v[64:65], v[48:49] op_sel_hi:[0,1]
	v_med3_f32 v48, v48, s70, v164
	v_med3_f32 v5, v49, s70, v164
	v_cvt_pk_fp8_f32 v42, v48, v5 op_sel:[0,0,1]
	v_mul_f32_e32 v48, 0x41000000, v165
	v_pk_fma_f32 v[38:39], v[38:39], s[36:37], v[158:159] op_sel_hi:[1,0,1]
	v_pk_fma_f32 v[34:35], v[34:35], s[36:37], v[154:155] op_sel_hi:[1,0,1]
	v_cvt_pk_fp8_f32 v51, v54, v65
	v_pk_mul_f32 v[38:39], v[48:49], v[38:39] op_sel_hi:[0,1]
	v_pk_mul_f32 v[34:35], v[48:49], v[34:35] op_sel_hi:[0,1]
	v_med3_f32 v5, v38, s70, v164
	v_med3_f32 v38, v34, s70, v164
	v_med3_f32 v39, v39, s70, v164
	v_mov_b32_e32 v34, v147
	v_cvt_pk_fp8_f32 v34, v5, v39
	v_med3_f32 v52, v52, s70, v164
	v_med3_f32 v53, v53, s70, v164
	v_pk_fma_f32 v[40:41], v[40:41], s[36:37], v[156:157] op_sel_hi:[1,0,1]
	v_pk_fma_f32 v[36:37], v[36:37], s[36:37], v[152:153] op_sel_hi:[1,0,1]
	v_cvt_pk_fp8_f32 v51, v52, v53 op_sel:[0,0,1]
	v_med3_f32 v52, v43, s70, v164
	v_mov_b32_e32 v43, v147
	v_pk_mul_f32 v[40:41], v[48:49], v[40:41] op_sel_hi:[0,1]
	v_pk_mul_f32 v[36:37], v[48:49], v[36:37] op_sel_hi:[0,1]
	v_med3_f32 v49, v35, s70, v164
	v_pk_fma_f32 v[30:31], v[30:31], s[36:37], v[150:151] op_sel_hi:[1,0,1]
	v_pk_fma_f32 v[26:27], v[26:27], s[36:37], v[6:7] op_sel_hi:[1,0,1]
	v_cvt_pk_fp8_f32 v43, v46, v52
	v_med3_f32 v40, v40, s70, v164
	v_med3_f32 v5, v41, s70, v164
	v_pk_mul_f32 v[30:31], v[48:49], v[30:31] op_sel_hi:[0,1]
	v_pk_mul_f32 v[26:27], v[48:49], v[26:27] op_sel_hi:[0,1]
	v_add_u32_e32 v62, 0x80, v4
	v_pk_fma_f32 v[44:45], v[44:45], s[36:37], v[2:3] op_sel_hi:[1,0,1]
	v_mov_b32_e32 v35, v147
	v_cvt_pk_fp8_f32 v34, v40, v5 op_sel:[0,0,1]
	v_med3_f32 v5, v30, s70, v164
	v_med3_f32 v30, v26, s70, v164
	v_med3_f32 v31, v31, s70, v164
	v_mov_b32_e32 v26, v147
	ds_read_b128 v[58:61], v123
	v_ashrrev_i32_e32 v63, 31, v62
	v_pk_mul_f32 v[44:45], v[64:65], v[44:45] op_sel_hi:[0,1]
	v_cvt_pk_fp8_f32 v35, v38, v49
	v_cvt_pk_fp8_f32 v26, v5, v31
	v_lshlrev_b64 v[62:63], 10, v[62:63]
	v_med3_f32 v44, v44, s70, v164
	v_med3_f32 v45, v45, s70, v164
	v_pk_fma_f32 v[32:33], v[32:33], s[36:37], v[8:9] op_sel_hi:[1,0,1]
	v_lshl_add_u64 v[62:63], s[16:17], 0, v[62:63]
	v_cvt_pk_fp8_f32 v43, v44, v45 op_sel:[0,0,1]
	v_pk_mul_f32 v[32:33], v[48:49], v[32:33] op_sel_hi:[0,1]
	v_lshl_add_u64 v[62:63], v[62:63], 0, s[6:7]
	v_med3_f32 v36, v36, s70, v164
	v_med3_f32 v37, v37, s70, v164
	v_med3_f32 v32, v32, s70, v164
	v_med3_f32 v5, v33, s70, v164
	v_lshl_add_u64 v[44:45], v[62:63], 0, v[146:147]
	v_cvt_pk_fp8_f32 v35, v36, v37 op_sel:[0,0,1]
	v_med3_f32 v36, v27, s70, v164
	v_mov_b32_e32 v27, v147
	v_cvt_pk_fp8_f32 v26, v32, v5 op_sel:[0,0,1]
	v_mul_f32_e32 v32, 0x41000000, v1
	v_pk_fma_f32 v[22:23], v[22:23], s[36:37], v[158:159] op_sel_hi:[1,0,1]
	v_pk_fma_f32 v[18:19], v[18:19], s[36:37], v[154:155] op_sel_hi:[1,0,1]
	s_waitcnt lgkmcnt(0)
	global_store_dwordx4 v[44:45], v[58:61], off
	v_cvt_pk_fp8_f32 v27, v30, v36
	v_pk_mul_f32 v[22:23], v[32:33], v[22:23] op_sel_hi:[0,1]
	v_pk_mul_f32 v[18:19], v[32:33], v[18:19] op_sel_hi:[0,1]
	ds_write2_b64 v122, v[50:51], v[42:43] offset1:4
	v_add_u32_e32 v46, 0x90, v4
	v_pk_fma_f32 v[28:29], v[28:29], s[36:37], v[2:3] op_sel_hi:[1,0,1]
	v_med3_f32 v1, v22, s70, v164
	v_med3_f32 v5, v18, s70, v164
	v_med3_f32 v22, v23, s70, v164
	v_med3_f32 v23, v19, s70, v164
	v_mov_b32_e32 v18, v147
	v_mov_b32_e32 v19, v147
	ds_read_b128 v[42:45], v123
	v_ashrrev_i32_e32 v47, 31, v46
	v_pk_mul_f32 v[28:29], v[48:49], v[28:29] op_sel_hi:[0,1]
	v_cvt_pk_fp8_f32 v18, v1, v22
	v_cvt_pk_fp8_f32 v19, v5, v23
	v_lshlrev_b64 v[46:47], 10, v[46:47]
	v_med3_f32 v28, v28, s70, v164
	v_med3_f32 v29, v29, s70, v164
	v_pk_fma_f32 v[24:25], v[24:25], s[36:37], v[156:157] op_sel_hi:[1,0,1]
	v_pk_fma_f32 v[20:21], v[20:21], s[36:37], v[152:153] op_sel_hi:[1,0,1]
	v_lshl_add_u64 v[46:47], s[16:17], 0, v[46:47]
	v_cvt_pk_fp8_f32 v27, v28, v29 op_sel:[0,0,1]
	v_pk_mul_f32 v[24:25], v[32:33], v[24:25] op_sel_hi:[0,1]
	v_pk_mul_f32 v[20:21], v[32:33], v[20:21] op_sel_hi:[0,1]
	v_pk_fma_f32 v[14:15], v[14:15], s[36:37], v[150:151] op_sel_hi:[1,0,1]
	v_pk_fma_f32 v[6:7], v[10:11], s[36:37], v[6:7] op_sel_hi:[1,0,1]
	v_lshl_add_u64 v[46:47], v[46:47], 0, s[6:7]
	v_med3_f32 v24, v24, s70, v164
	v_med3_f32 v20, v20, s70, v164
	v_med3_f32 v1, v25, s70, v164
	v_med3_f32 v5, v21, s70, v164
	v_pk_mul_f32 v[14:15], v[32:33], v[14:15] op_sel_hi:[0,1]
	v_pk_mul_f32 v[6:7], v[32:33], v[6:7] op_sel_hi:[0,1]
	v_lshl_add_u64 v[28:29], v[46:47], 0, v[146:147]
	v_cvt_pk_fp8_f32 v18, v24, v1 op_sel:[0,0,1]
	v_cvt_pk_fp8_f32 v19, v20, v5 op_sel:[0,0,1]
	v_med3_f32 v1, v14, s70, v164
	v_med3_f32 v5, v6, s70, v164
	v_med3_f32 v10, v15, s70, v164
	v_med3_f32 v11, v7, s70, v164
	v_mov_b32_e32 v6, v147
	v_mov_b32_e32 v7, v147
	s_waitcnt lgkmcnt(0)
	global_store_dwordx4 v[28:29], v[42:45], off
	v_cvt_pk_fp8_f32 v6, v1, v10
	v_cvt_pk_fp8_f32 v7, v5, v11
	ds_write2_b64 v122, v[34:35], v[26:27] offset1:4
	v_add_u32_e32 v30, 0xa0, v4
	v_pk_fma_f32 v[8:9], v[16:17], s[36:37], v[8:9] op_sel_hi:[1,0,1]
	v_pk_fma_f32 v[2:3], v[12:13], s[36:37], v[2:3] op_sel_hi:[1,0,1]
	ds_read_b128 v[26:29], v123
	v_ashrrev_i32_e32 v31, 31, v30
	v_pk_mul_f32 v[8:9], v[32:33], v[8:9] op_sel_hi:[0,1]
	v_pk_mul_f32 v[2:3], v[32:33], v[2:3] op_sel_hi:[0,1]
	v_lshlrev_b64 v[30:31], 10, v[30:31]
	v_med3_f32 v8, v8, s70, v164
	v_med3_f32 v2, v2, s70, v164
	v_med3_f32 v1, v9, s70, v164
	v_med3_f32 v3, v3, s70, v164
	v_lshl_add_u64 v[30:31], s[16:17], 0, v[30:31]
	v_cvt_pk_fp8_f32 v6, v8, v1 op_sel:[0,0,1]
	v_cvt_pk_fp8_f32 v7, v2, v3 op_sel:[0,0,1]
	v_lshl_add_u64 v[30:31], v[30:31], 0, s[6:7]
	v_lshl_add_u64 v[2:3], v[30:31], 0, v[146:147]
	s_waitcnt lgkmcnt(0)
	global_store_dwordx4 v[2:3], v[26:29], off
	ds_write2_b64 v122, v[18:19], v[6:7] offset1:4
	v_add_u32_e32 v2, 0xb0, v4
	ds_read_b128 v[6:9], v123
	v_ashrrev_i32_e32 v3, 31, v2
	v_lshlrev_b64 v[2:3], 10, v[2:3]
	v_lshl_add_u64 v[2:3], s[16:17], 0, v[2:3]
	v_lshl_add_u64 v[2:3], v[2:3], 0, s[6:7]
	v_lshl_add_u64 v[2:3], v[2:3], 0, v[146:147]
	s_waitcnt lgkmcnt(0)
	global_store_dwordx4 v[2:3], v[6:9], off
	s_and_b64 vcc, exec, s[8:9]
	s_mov_b64 s[6:7], -1
	s_cbranch_vccnz .LBB0_1616
	v_mov_b32_e32 v12, v0
	s_lshl_b32 s7, s40, 8
	v_readfirstlane_b32 s6, v12
	s_and_b32 s8, s6, 0xc0
	s_ashr_i32 s6, s6, 2
	s_andn2_b32 s6, s6, 63
	s_add_i32 s6, s6, s7
	v_and_or_b32 v2, v12, 15, s6
	v_ashrrev_i32_e32 v3, 31, v2
	s_lshl_b64 s[6:7], s[42:43], 11
	v_lshl_add_u64 v[4:5], v[2:3], 2, s[12:13]
	v_add_u32_e32 v6, 0x80, v2
	v_add_u32_e32 v8, 0x90, v2
	v_add_u32_e32 v10, 0xa0, v2
	v_add_u32_e32 v2, 0xb0, v2
	s_add_u32 s9, s56, s6
	v_ashrrev_i32_e32 v7, 31, v6
	v_ashrrev_i32_e32 v9, 31, v8
	v_ashrrev_i32_e32 v11, 31, v10
	v_ashrrev_i32_e32 v3, 31, v2
	s_addc_u32 s39, s57, s7
	s_lshl_b32 s6, s38, 8
	v_lshl_add_u64 v[6:7], v[6:7], 2, s[12:13]
	v_lshl_add_u64 v[8:9], v[8:9], 2, s[12:13]
	v_lshl_add_u64 v[10:11], v[10:11], 2, s[12:13]
	v_lshl_add_u64 v[2:3], v[2:3], 2, s[12:13]
	global_load_dword v146, v[4:5], off
	global_load_dword v170, v[4:5], off offset:64
	global_load_dword v169, v[4:5], off offset:128
	global_load_dword v168, v[4:5], off offset:192
	global_load_dword v167, v[6:7], off
	global_load_dword v166, v[8:9], off
	global_load_dword v165, v[10:11], off
	global_load_dword v1, v[2:3], off
	s_ashr_i32 s7, s6, 31
	s_lshl_b64 s[6:7], s[6:7], 1
	s_add_u32 s6, s9, s6
	s_addc_u32 s7, s39, s7
	s_lshl_b32 s8, s8, 1
	s_add_u32 s6, s6, s8
	s_addc_u32 s7, s7, 0
	v_and_b32_e32 v2, 48, v12
	global_load_dwordx4 v[6:9], v2, s[6:7]
	s_nop 0
	global_load_dwordx4 v[2:5], v2, s[6:7] offset:64
	s_andn2_b64 vcc, exec, s[14:15]
	s_cbranch_vccnz .LBB0_1615
	s_barrier
	s_branch .LBB0_1615

.LBB0_3429:
	v_lshlrev_b32_e32 v158, 16, v6
	v_and_b32_e32 v159, 0xffff0000, v6
	v_lshlrev_b32_e32 v154, 16, v8
	v_and_b32_e32 v155, 0xffff0000, v8
	v_lshlrev_b32_e32 v156, 16, v7
	v_and_b32_e32 v157, 0xffff0000, v7
	v_lshlrev_b32_e32 v152, 16, v9
	v_and_b32_e32 v153, 0xffff0000, v9
	s_waitcnt vmcnt(10)
	v_lshlrev_b32_e32 v6, 16, v4
	v_and_b32_e32 v7, 0xffff0000, v4
	v_mul_f32_e32 v4, 0x41000000, v146
	v_pk_fma_f32 v[134:135], v[134:135], s[38:39], v[158:159] op_sel_hi:[1,0,1]
	v_pk_fma_f32 v[130:131], v[130:131], s[38:39], v[154:155] op_sel_hi:[1,0,1]
	v_pk_fma_f32 v[136:137], v[136:137], s[38:39], v[156:157] op_sel_hi:[1,0,1]
	v_pk_mul_f32 v[134:135], v[4:5], v[134:135] op_sel_hi:[0,1]
	v_pk_fma_f32 v[132:133], v[132:133], s[38:39], v[152:153] op_sel_hi:[1,0,1]
	v_pk_mul_f32 v[130:131], v[4:5], v[130:131] op_sel_hi:[0,1]
	v_lshlrev_b32_e32 v150, 16, v2
	v_and_b32_e32 v151, 0xffff0000, v2
	v_lshlrev_b32_e32 v8, 16, v3
	v_and_b32_e32 v9, 0xffff0000, v3
	v_lshlrev_b32_e32 v2, 16, v5
	v_and_b32_e32 v3, 0xffff0000, v5
	v_pk_mul_f32 v[136:137], v[4:5], v[136:137] op_sel_hi:[0,1]
	v_pk_mul_f32 v[132:133], v[4:5], v[132:133] op_sel_hi:[0,1]
	v_med3_f32 v5, v134, s75, v164
	v_med3_f32 v134, v130, s75, v164
	v_med3_f32 v135, v135, s75, v164
	v_mov_b32_e32 v130, 0
	v_cvt_pk_fp8_f32 v130, v5, v135
	v_med3_f32 v136, v136, s75, v164
	v_med3_f32 v5, v137, s75, v164
	v_pk_fma_f32 v[126:127], v[126:127], s[38:39], v[150:151] op_sel_hi:[1,0,1]
	v_pk_fma_f32 v[128:129], v[128:129], s[38:39], v[8:9] op_sel_hi:[1,0,1]
	v_pk_fma_f32 v[122:123], v[122:123], s[38:39], v[6:7] op_sel_hi:[1,0,1]
	v_pk_fma_f32 v[124:125], v[124:125], s[38:39], v[2:3] op_sel_hi:[1,0,1]
	v_cvt_pk_fp8_f32 v130, v136, v5 op_sel:[0,0,1]
	v_pk_mul_f32 v[128:129], v[4:5], v[128:129] op_sel_hi:[0,1]
	v_pk_mul_f32 v[126:127], v[4:5], v[126:127] op_sel_hi:[0,1]
	v_pk_mul_f32 v[124:125], v[4:5], v[124:125] op_sel_hi:[0,1]
	v_pk_mul_f32 v[4:5], v[4:5], v[122:123] op_sel_hi:[0,1]
	v_med3_f32 v146, v131, s75, v164
	v_mov_b32_e32 v131, 0
	v_med3_f32 v122, v126, s75, v164
	v_med3_f32 v123, v4, s75, v164
	v_med3_f32 v126, v127, s75, v164
	v_med3_f32 v127, v5, s75, v164
	v_mov_b32_e32 v4, 0
	v_mov_b32_e32 v5, 0
	v_cvt_pk_fp8_f32 v131, v134, v146
	v_cvt_pk_fp8_f32 v4, v122, v126
	v_cvt_pk_fp8_f32 v5, v123, v127
	v_mov_b32_e32 v171, v0
	v_med3_f32 v132, v132, s75, v164
	v_readfirstlane_b32 s41, v171
	s_lshr_b32 s8, s41, 6
	v_med3_f32 v133, v133, s75, v164
	v_med3_f32 v128, v128, s75, v164
	v_med3_f32 v124, v124, s75, v164
	v_med3_f32 v122, v129, s75, v164
	v_med3_f32 v123, v125, s75, v164
	s_mulk_i32 s8, 0xb00
	v_cvt_pk_fp8_f32 v131, v132, v133 op_sel:[0,0,1]
	v_cvt_pk_fp8_f32 v4, v128, v122 op_sel:[0,0,1]
	v_cvt_pk_fp8_f32 v5, v124, v123 op_sel:[0,0,1]
	s_add_i32 s8, s8, 0
	v_and_b32_e32 v172, 15, v171
	v_lshrrev_b32_e32 v123, 1, v171
	s_add_i32 s43, s8, 0x20000
	v_mul_u32_u24_e32 v122, 0x50, v172
	v_and_b32_e32 v123, 24, v123
	v_add3_u32 v122, s43, v122, v123
	s_and_b32 s9, s41, 0xc0
	ds_write2_b64 v122, v[130:131], v[4:5] offset1:4
	v_bfe_u32 v4, v171, 2, 4
	s_ashr_i32 s41, s41, 2
	v_mul_u32_u24_e32 v5, 0x50, v4
	v_lshlrev_b32_e32 v123, 4, v171
	s_andn2_b32 s41, s41, 63
	v_lshl_or_b32 v4, s50, 8, v4
	v_and_b32_e32 v146, 48, v123
	v_add_u32_e32 v4, s41, v4
	v_mul_f32_e32 v130, 0x41000000, v170
	v_pk_fma_f32 v[118:119], v[118:119], s[38:39], v[158:159] op_sel_hi:[1,0,1]
	v_pk_fma_f32 v[114:115], v[114:115], s[38:39], v[154:155] op_sel_hi:[1,0,1]
	v_add3_u32 v123, s43, v5, v146
	v_ashrrev_i32_e32 v5, 31, v4
	v_pk_mul_f32 v[118:119], v[130:131], v[118:119] op_sel_hi:[0,1]
	v_pk_mul_f32 v[114:115], v[130:131], v[114:115] op_sel_hi:[0,1]
	v_lshlrev_b64 v[128:129], 10, v[4:5]
	v_med3_f32 v5, v118, s75, v164
	v_med3_f32 v118, v114, s75, v164
	v_med3_f32 v119, v119, s75, v164
	v_mov_b32_e32 v114, v147
	v_cvt_pk_fp8_f32 v114, v5, v119
	v_pk_fma_f32 v[120:121], v[120:121], s[38:39], v[156:157] op_sel_hi:[1,0,1]
	v_pk_fma_f32 v[116:117], v[116:117], s[38:39], v[152:153] op_sel_hi:[1,0,1]
	v_pk_mul_f32 v[120:121], v[130:131], v[120:121] op_sel_hi:[0,1]
	v_pk_mul_f32 v[116:117], v[130:131], v[116:117] op_sel_hi:[0,1]
	v_med3_f32 v131, v115, s75, v164
	v_pk_fma_f32 v[110:111], v[110:111], s[38:39], v[150:151] op_sel_hi:[1,0,1]
	v_pk_fma_f32 v[106:107], v[106:107], s[38:39], v[6:7] op_sel_hi:[1,0,1]
	v_med3_f32 v120, v120, s75, v164
	v_med3_f32 v5, v121, s75, v164
	v_pk_mul_f32 v[110:111], v[130:131], v[110:111] op_sel_hi:[0,1]
	v_pk_mul_f32 v[106:107], v[130:131], v[106:107] op_sel_hi:[0,1]
	v_cvt_pk_fp8_f32 v114, v120, v5 op_sel:[0,0,1]
	v_med3_f32 v5, v110, s75, v164
	v_med3_f32 v110, v106, s75, v164
	v_med3_f32 v111, v111, s75, v164
	v_mov_b32_e32 v106, v147
	v_cvt_pk_fp8_f32 v106, v5, v111
	v_pk_fma_f32 v[112:113], v[112:113], s[38:39], v[8:9] op_sel_hi:[1,0,1]
	v_mov_b32_e32 v115, v147
	v_pk_mul_f32 v[112:113], v[130:131], v[112:113] op_sel_hi:[0,1]
	v_med3_f32 v112, v112, s75, v164
	v_med3_f32 v5, v113, s75, v164
	v_cvt_pk_fp8_f32 v106, v112, v5 op_sel:[0,0,1]
	v_mul_f32_e32 v112, 0x41000000, v169
	v_pk_fma_f32 v[102:103], v[102:103], s[38:39], v[158:159] op_sel_hi:[1,0,1]
	v_pk_fma_f32 v[98:99], v[98:99], s[38:39], v[154:155] op_sel_hi:[1,0,1]
	v_cvt_pk_fp8_f32 v115, v118, v131
	v_pk_mul_f32 v[102:103], v[112:113], v[102:103] op_sel_hi:[0,1]
	v_pk_mul_f32 v[98:99], v[112:113], v[98:99] op_sel_hi:[0,1]
	v_med3_f32 v5, v102, s75, v164
	v_med3_f32 v102, v98, s75, v164
	v_med3_f32 v103, v103, s75, v164
	v_mov_b32_e32 v98, v147
	v_cvt_pk_fp8_f32 v98, v5, v103
	v_med3_f32 v116, v116, s75, v164
	v_med3_f32 v117, v117, s75, v164
	v_pk_fma_f32 v[104:105], v[104:105], s[38:39], v[156:157] op_sel_hi:[1,0,1]
	v_pk_fma_f32 v[100:101], v[100:101], s[38:39], v[152:153] op_sel_hi:[1,0,1]
	v_cvt_pk_fp8_f32 v115, v116, v117 op_sel:[0,0,1]
	v_med3_f32 v116, v107, s75, v164
	v_mov_b32_e32 v107, v147
	v_pk_mul_f32 v[104:105], v[112:113], v[104:105] op_sel_hi:[0,1]
	v_pk_mul_f32 v[100:101], v[112:113], v[100:101] op_sel_hi:[0,1]
	v_med3_f32 v113, v99, s75, v164
	v_pk_fma_f32 v[94:95], v[94:95], s[38:39], v[150:151] op_sel_hi:[1,0,1]
	v_pk_fma_f32 v[90:91], v[90:91], s[38:39], v[6:7] op_sel_hi:[1,0,1]
	v_cvt_pk_fp8_f32 v107, v110, v116
	v_med3_f32 v104, v104, s75, v164
	v_med3_f32 v5, v105, s75, v164
	v_pk_mul_f32 v[94:95], v[112:113], v[94:95] op_sel_hi:[0,1]
	v_pk_mul_f32 v[90:91], v[112:113], v[90:91] op_sel_hi:[0,1]
	v_pk_fma_f32 v[108:109], v[108:109], s[38:39], v[2:3] op_sel_hi:[1,0,1]
	v_mov_b32_e32 v99, v147
	v_cvt_pk_fp8_f32 v98, v104, v5 op_sel:[0,0,1]
	v_med3_f32 v5, v94, s75, v164
	v_med3_f32 v94, v90, s75, v164
	v_med3_f32 v95, v95, s75, v164
	v_mov_b32_e32 v90, v147
	s_lshl_b32 s8, s62, 8
	ds_read_b128 v[124:127], v123
	v_pk_mul_f32 v[108:109], v[130:131], v[108:109] op_sel_hi:[0,1]
	v_cvt_pk_fp8_f32 v99, v102, v113
	v_cvt_pk_fp8_f32 v90, v5, v95
	s_or_b32 s8, s9, s8
	v_med3_f32 v108, v108, s75, v164
	v_med3_f32 v109, v109, s75, v164
	v_pk_fma_f32 v[96:97], v[96:97], s[38:39], v[8:9] op_sel_hi:[1,0,1]
	s_ashr_i32 s9, s8, 31
	v_lshl_add_u64 v[128:129], s[16:17], 0, v[128:129]
	v_cvt_pk_fp8_f32 v107, v108, v109 op_sel:[0,0,1]
	v_pk_mul_f32 v[96:97], v[112:113], v[96:97] op_sel_hi:[0,1]
	v_lshl_add_u64 v[128:129], v[128:129], 0, s[8:9]
	v_med3_f32 v100, v100, s75, v164
	v_med3_f32 v101, v101, s75, v164
	v_med3_f32 v96, v96, s75, v164
	v_med3_f32 v5, v97, s75, v164
	v_lshl_add_u64 v[108:109], v[128:129], 0, v[146:147]
	v_cvt_pk_fp8_f32 v99, v100, v101 op_sel:[0,0,1]
	v_med3_f32 v100, v91, s75, v164
	v_mov_b32_e32 v91, v147
	v_cvt_pk_fp8_f32 v90, v96, v5 op_sel:[0,0,1]
	v_mul_f32_e32 v96, 0x41000000, v168
	v_pk_fma_f32 v[78:79], v[78:79], s[38:39], v[158:159] op_sel_hi:[1,0,1]
	v_pk_fma_f32 v[74:75], v[74:75], s[38:39], v[154:155] op_sel_hi:[1,0,1]
	s_waitcnt lgkmcnt(0)
	global_store_dwordx4 v[108:109], v[124:127], off
	v_cvt_pk_fp8_f32 v91, v94, v100
	v_pk_fma_f32 v[80:81], v[80:81], s[38:39], v[156:157] op_sel_hi:[1,0,1]
	v_pk_mul_f32 v[78:79], v[96:97], v[78:79] op_sel_hi:[0,1]
	v_pk_fma_f32 v[76:77], v[76:77], s[38:39], v[152:153] op_sel_hi:[1,0,1]
	v_pk_mul_f32 v[74:75], v[96:97], v[74:75] op_sel_hi:[0,1]
	ds_write2_b64 v122, v[114:115], v[106:107] offset1:4
	v_or_b32_e32 v110, 16, v4
	v_pk_fma_f32 v[92:93], v[92:93], s[38:39], v[2:3] op_sel_hi:[1,0,1]
	v_pk_mul_f32 v[80:81], v[96:97], v[80:81] op_sel_hi:[0,1]
	v_pk_mul_f32 v[76:77], v[96:97], v[76:77] op_sel_hi:[0,1]
	v_med3_f32 v5, v78, s75, v164
	v_med3_f32 v78, v74, s75, v164
	v_med3_f32 v79, v79, s75, v164
	v_med3_f32 v97, v75, s75, v164
	v_mov_b32_e32 v74, v147
	v_mov_b32_e32 v75, v147
	ds_read_b128 v[106:109], v123
	v_ashrrev_i32_e32 v111, 31, v110
	v_pk_mul_f32 v[92:93], v[112:113], v[92:93] op_sel_hi:[0,1]
	v_cvt_pk_fp8_f32 v74, v5, v79
	v_cvt_pk_fp8_f32 v75, v78, v97
	v_lshlrev_b64 v[110:111], 10, v[110:111]
	v_med3_f32 v92, v92, s75, v164
	v_med3_f32 v93, v93, s75, v164
	v_lshl_add_u64 v[110:111], s[16:17], 0, v[110:111]
	v_cvt_pk_fp8_f32 v91, v92, v93 op_sel:[0,0,1]
	v_pk_fma_f32 v[62:63], v[62:63], s[38:39], v[150:151] op_sel_hi:[1,0,1]
	v_pk_fma_f32 v[58:59], v[58:59], s[38:39], v[6:7] op_sel_hi:[1,0,1]
	v_lshl_add_u64 v[110:111], v[110:111], 0, s[8:9]
	v_med3_f32 v80, v80, s75, v164
	v_med3_f32 v76, v76, s75, v164
	v_med3_f32 v5, v81, s75, v164
	v_med3_f32 v77, v77, s75, v164
	v_pk_mul_f32 v[62:63], v[96:97], v[62:63] op_sel_hi:[0,1]
	v_pk_mul_f32 v[58:59], v[96:97], v[58:59] op_sel_hi:[0,1]
	v_lshl_add_u64 v[92:93], v[110:111], 0, v[146:147]
	v_cvt_pk_fp8_f32 v74, v80, v5 op_sel:[0,0,1]
	v_cvt_pk_fp8_f32 v75, v76, v77 op_sel:[0,0,1]
	v_med3_f32 v5, v62, s75, v164
	v_med3_f32 v62, v58, s75, v164
	v_med3_f32 v63, v63, s75, v164
	v_med3_f32 v76, v59, s75, v164
	v_mov_b32_e32 v58, v147
	v_mov_b32_e32 v59, v147
	s_waitcnt lgkmcnt(0)
	global_store_dwordx4 v[92:93], v[106:109], off
	v_cvt_pk_fp8_f32 v58, v5, v63
	v_cvt_pk_fp8_f32 v59, v62, v76
	ds_write2_b64 v122, v[98:99], v[90:91] offset1:4
	v_or_b32_e32 v94, 32, v4
	v_pk_fma_f32 v[64:65], v[64:65], s[38:39], v[8:9] op_sel_hi:[1,0,1]
	v_pk_fma_f32 v[60:61], v[60:61], s[38:39], v[2:3] op_sel_hi:[1,0,1]
	ds_read_b128 v[90:93], v123
	v_ashrrev_i32_e32 v95, 31, v94
	v_pk_mul_f32 v[64:65], v[96:97], v[64:65] op_sel_hi:[0,1]
	v_pk_mul_f32 v[60:61], v[96:97], v[60:61] op_sel_hi:[0,1]
	v_lshlrev_b64 v[94:95], 10, v[94:95]
	v_med3_f32 v64, v64, s75, v164
	v_med3_f32 v60, v60, s75, v164
	v_med3_f32 v5, v65, s75, v164
	v_med3_f32 v61, v61, s75, v164
	v_lshl_add_u64 v[94:95], s[16:17], 0, v[94:95]
	v_cvt_pk_fp8_f32 v58, v64, v5 op_sel:[0,0,1]
	v_cvt_pk_fp8_f32 v59, v60, v61 op_sel:[0,0,1]
	v_lshl_add_u64 v[94:95], v[94:95], 0, s[8:9]
	v_lshl_add_u64 v[60:61], v[94:95], 0, v[146:147]
	s_waitcnt lgkmcnt(0)
	global_store_dwordx4 v[60:61], v[90:93], off
	ds_write2_b64 v122, v[74:75], v[58:59] offset1:4
	v_mul_f32_e32 v64, 0x41000000, v167
	v_pk_fma_f32 v[74:75], v[86:87], s[38:39], v[158:159] op_sel_hi:[1,0,1]
	v_pk_fma_f32 v[78:79], v[82:83], s[38:39], v[154:155] op_sel_hi:[1,0,1]
	v_pk_mul_f32 v[74:75], v[64:65], v[74:75] op_sel_hi:[0,1]
	v_pk_fma_f32 v[76:77], v[88:89], s[38:39], v[156:157] op_sel_hi:[1,0,1]
	v_pk_fma_f32 v[80:81], v[84:85], s[38:39], v[152:153] op_sel_hi:[1,0,1]
	v_pk_mul_f32 v[78:79], v[64:65], v[78:79] op_sel_hi:[0,1]
	v_med3_f32 v5, v74, s75, v164
	v_med3_f32 v75, v75, s75, v164
	v_mov_b32_e32 v74, v147
	v_pk_mul_f32 v[76:77], v[64:65], v[76:77] op_sel_hi:[0,1]
	v_pk_mul_f32 v[80:81], v[64:65], v[80:81] op_sel_hi:[0,1]
	v_med3_f32 v65, v78, s75, v164
	v_med3_f32 v78, v79, s75, v164
	v_cvt_pk_fp8_f32 v74, v5, v75
	v_mov_b32_e32 v75, v147
	v_cvt_pk_fp8_f32 v75, v65, v78
	v_med3_f32 v79, v80, s75, v164
	v_med3_f32 v65, v81, s75, v164
	v_pk_fma_f32 v[70:71], v[70:71], s[38:39], v[150:151] op_sel_hi:[1,0,1]
	v_pk_fma_f32 v[72:73], v[72:73], s[38:39], v[8:9] op_sel_hi:[1,0,1]
	v_pk_fma_f32 v[66:67], v[66:67], s[38:39], v[6:7] op_sel_hi:[1,0,1]
	v_pk_fma_f32 v[68:69], v[68:69], s[38:39], v[2:3] op_sel_hi:[1,0,1]
	v_med3_f32 v76, v76, s75, v164
	v_med3_f32 v5, v77, s75, v164
	v_cvt_pk_fp8_f32 v75, v79, v65 op_sel:[0,0,1]
	v_pk_mul_f32 v[72:73], v[64:65], v[72:73] op_sel_hi:[0,1]
	v_pk_mul_f32 v[70:71], v[64:65], v[70:71] op_sel_hi:[0,1]
	v_pk_mul_f32 v[68:69], v[64:65], v[68:69] op_sel_hi:[0,1]
	v_pk_mul_f32 v[64:65], v[64:65], v[66:67] op_sel_hi:[0,1]
	v_cvt_pk_fp8_f32 v74, v76, v5 op_sel:[0,0,1]
	v_med3_f32 v5, v70, s75, v164
	v_med3_f32 v66, v64, s75, v164
	v_med3_f32 v67, v71, s75, v164
	v_med3_f32 v70, v65, s75, v164
	v_mov_b32_e32 v64, v147
	v_mov_b32_e32 v65, v147
	v_cvt_pk_fp8_f32 v64, v5, v67
	v_cvt_pk_fp8_f32 v65, v66, v70
	v_or_b32_e32 v62, 48, v4
	ds_read_b128 v[58:61], v123
	v_ashrrev_i32_e32 v63, 31, v62
	v_lshlrev_b64 v[62:63], 10, v[62:63]
	v_med3_f32 v71, v72, s75, v164
	v_med3_f32 v68, v68, s75, v164
	v_med3_f32 v5, v73, s75, v164
	v_med3_f32 v66, v69, s75, v164
	v_lshl_add_u64 v[62:63], s[16:17], 0, v[62:63]
	v_cvt_pk_fp8_f32 v64, v71, v5 op_sel:[0,0,1]
	v_cvt_pk_fp8_f32 v65, v68, v66 op_sel:[0,0,1]
	v_lshl_add_u64 v[62:63], v[62:63], 0, s[8:9]
	v_lshl_add_u64 v[62:63], v[62:63], 0, v[146:147]
	s_waitcnt lgkmcnt(0)
	global_store_dwordx4 v[62:63], v[58:61], off
	ds_write2_b64 v122, v[74:75], v[64:65] offset1:4
	v_mul_f32_e32 v64, 0x41000000, v166
	v_pk_fma_f32 v[54:55], v[54:55], s[38:39], v[158:159] op_sel_hi:[1,0,1]
	v_pk_fma_f32 v[50:51], v[50:51], s[38:39], v[154:155] op_sel_hi:[1,0,1]
	v_pk_mul_f32 v[54:55], v[64:65], v[54:55] op_sel_hi:[0,1]
	v_pk_mul_f32 v[50:51], v[64:65], v[50:51] op_sel_hi:[0,1]
	v_med3_f32 v5, v54, s75, v164
	v_med3_f32 v54, v50, s75, v164
	v_med3_f32 v55, v55, s75, v164
	v_mov_b32_e32 v50, v147
	v_cvt_pk_fp8_f32 v50, v5, v55
	v_pk_fma_f32 v[56:57], v[56:57], s[38:39], v[156:157] op_sel_hi:[1,0,1]
	v_pk_fma_f32 v[52:53], v[52:53], s[38:39], v[152:153] op_sel_hi:[1,0,1]
	v_pk_mul_f32 v[56:57], v[64:65], v[56:57] op_sel_hi:[0,1]
	v_pk_mul_f32 v[52:53], v[64:65], v[52:53] op_sel_hi:[0,1]
	v_med3_f32 v65, v51, s75, v164
	v_pk_fma_f32 v[46:47], v[46:47], s[38:39], v[150:151] op_sel_hi:[1,0,1]
	v_pk_fma_f32 v[42:43], v[42:43], s[38:39], v[6:7] op_sel_hi:[1,0,1]
	v_med3_f32 v56, v56, s75, v164
	v_med3_f32 v5, v57, s75, v164
	v_pk_mul_f32 v[46:47], v[64:65], v[46:47] op_sel_hi:[0,1]
	v_pk_mul_f32 v[42:43], v[64:65], v[42:43] op_sel_hi:[0,1]
	v_cvt_pk_fp8_f32 v50, v56, v5 op_sel:[0,0,1]
	v_med3_f32 v5, v46, s75, v164
	v_med3_f32 v46, v42, s75, v164
	v_med3_f32 v47, v47, s75, v164
	v_mov_b32_e32 v42, v147
	v_cvt_pk_fp8_f32 v42, v5, v47
	v_pk_fma_f32 v[48:49], v[48:49], s[38:39], v[8:9] op_sel_hi:[1,0,1]
	v_mov_b32_e32 v51, v147
	v_pk_mul_f32 v[48:49], v[64:65], v[48:49] op_sel_hi:[0,1]
	v_med3_f32 v48, v48, s75, v164
	v_med3_f32 v5, v49, s75, v164
	v_cvt_pk_fp8_f32 v42, v48, v5 op_sel:[0,0,1]
	v_mul_f32_e32 v48, 0x41000000, v165
	v_pk_fma_f32 v[38:39], v[38:39], s[38:39], v[158:159] op_sel_hi:[1,0,1]
	v_pk_fma_f32 v[34:35], v[34:35], s[38:39], v[154:155] op_sel_hi:[1,0,1]
	v_cvt_pk_fp8_f32 v51, v54, v65
	v_pk_mul_f32 v[38:39], v[48:49], v[38:39] op_sel_hi:[0,1]
	v_pk_mul_f32 v[34:35], v[48:49], v[34:35] op_sel_hi:[0,1]
	v_med3_f32 v5, v38, s75, v164
	v_med3_f32 v38, v34, s75, v164
	v_med3_f32 v39, v39, s75, v164
	v_mov_b32_e32 v34, v147
	v_cvt_pk_fp8_f32 v34, v5, v39
	v_med3_f32 v52, v52, s75, v164
	v_med3_f32 v53, v53, s75, v164
	v_pk_fma_f32 v[40:41], v[40:41], s[38:39], v[156:157] op_sel_hi:[1,0,1]
	v_pk_fma_f32 v[36:37], v[36:37], s[38:39], v[152:153] op_sel_hi:[1,0,1]
	v_cvt_pk_fp8_f32 v51, v52, v53 op_sel:[0,0,1]
	v_med3_f32 v52, v43, s75, v164
	v_mov_b32_e32 v43, v147
	v_pk_mul_f32 v[40:41], v[48:49], v[40:41] op_sel_hi:[0,1]
	v_pk_mul_f32 v[36:37], v[48:49], v[36:37] op_sel_hi:[0,1]
	v_med3_f32 v49, v35, s75, v164
	v_pk_fma_f32 v[30:31], v[30:31], s[38:39], v[150:151] op_sel_hi:[1,0,1]
	v_pk_fma_f32 v[26:27], v[26:27], s[38:39], v[6:7] op_sel_hi:[1,0,1]
	v_cvt_pk_fp8_f32 v43, v46, v52
	v_med3_f32 v40, v40, s75, v164
	v_med3_f32 v5, v41, s75, v164
	v_pk_mul_f32 v[30:31], v[48:49], v[30:31] op_sel_hi:[0,1]
	v_pk_mul_f32 v[26:27], v[48:49], v[26:27] op_sel_hi:[0,1]
	v_add_u32_e32 v62, 0x80, v4
	v_pk_fma_f32 v[44:45], v[44:45], s[38:39], v[2:3] op_sel_hi:[1,0,1]
	v_mov_b32_e32 v35, v147
	v_cvt_pk_fp8_f32 v34, v40, v5 op_sel:[0,0,1]
	v_med3_f32 v5, v30, s75, v164
	v_med3_f32 v30, v26, s75, v164
	v_med3_f32 v31, v31, s75, v164
	v_mov_b32_e32 v26, v147
	ds_read_b128 v[58:61], v123
	v_ashrrev_i32_e32 v63, 31, v62
	v_pk_mul_f32 v[44:45], v[64:65], v[44:45] op_sel_hi:[0,1]
	v_cvt_pk_fp8_f32 v35, v38, v49
	v_cvt_pk_fp8_f32 v26, v5, v31
	v_lshlrev_b64 v[62:63], 10, v[62:63]
	v_med3_f32 v44, v44, s75, v164
	v_med3_f32 v45, v45, s75, v164
	v_pk_fma_f32 v[32:33], v[32:33], s[38:39], v[8:9] op_sel_hi:[1,0,1]
	v_lshl_add_u64 v[62:63], s[16:17], 0, v[62:63]
	v_cvt_pk_fp8_f32 v43, v44, v45 op_sel:[0,0,1]
	v_pk_mul_f32 v[32:33], v[48:49], v[32:33] op_sel_hi:[0,1]
	v_lshl_add_u64 v[62:63], v[62:63], 0, s[8:9]
	v_med3_f32 v36, v36, s75, v164
	v_med3_f32 v37, v37, s75, v164
	v_med3_f32 v32, v32, s75, v164
	v_med3_f32 v5, v33, s75, v164
	v_lshl_add_u64 v[44:45], v[62:63], 0, v[146:147]
	v_cvt_pk_fp8_f32 v35, v36, v37 op_sel:[0,0,1]
	v_med3_f32 v36, v27, s75, v164
	v_mov_b32_e32 v27, v147
	v_cvt_pk_fp8_f32 v26, v32, v5 op_sel:[0,0,1]
	v_mul_f32_e32 v32, 0x41000000, v1
	v_pk_fma_f32 v[22:23], v[22:23], s[38:39], v[158:159] op_sel_hi:[1,0,1]
	v_pk_fma_f32 v[18:19], v[18:19], s[38:39], v[154:155] op_sel_hi:[1,0,1]
	s_waitcnt lgkmcnt(0)
	global_store_dwordx4 v[44:45], v[58:61], off
	v_cvt_pk_fp8_f32 v27, v30, v36
	v_pk_mul_f32 v[22:23], v[32:33], v[22:23] op_sel_hi:[0,1]
	v_pk_mul_f32 v[18:19], v[32:33], v[18:19] op_sel_hi:[0,1]
	ds_write2_b64 v122, v[50:51], v[42:43] offset1:4
	v_add_u32_e32 v46, 0x90, v4
	v_pk_fma_f32 v[28:29], v[28:29], s[38:39], v[2:3] op_sel_hi:[1,0,1]
	v_med3_f32 v1, v22, s75, v164
	v_med3_f32 v5, v18, s75, v164
	v_med3_f32 v22, v23, s75, v164
	v_med3_f32 v23, v19, s75, v164
	v_mov_b32_e32 v18, v147
	v_mov_b32_e32 v19, v147
	ds_read_b128 v[42:45], v123
	v_ashrrev_i32_e32 v47, 31, v46
	v_pk_mul_f32 v[28:29], v[48:49], v[28:29] op_sel_hi:[0,1]
	v_cvt_pk_fp8_f32 v18, v1, v22
	v_cvt_pk_fp8_f32 v19, v5, v23
	v_lshlrev_b64 v[46:47], 10, v[46:47]
	v_med3_f32 v28, v28, s75, v164
	v_med3_f32 v29, v29, s75, v164
	v_pk_fma_f32 v[24:25], v[24:25], s[38:39], v[156:157] op_sel_hi:[1,0,1]
	v_pk_fma_f32 v[20:21], v[20:21], s[38:39], v[152:153] op_sel_hi:[1,0,1]
	v_lshl_add_u64 v[46:47], s[16:17], 0, v[46:47]
	v_cvt_pk_fp8_f32 v27, v28, v29 op_sel:[0,0,1]
	v_pk_mul_f32 v[24:25], v[32:33], v[24:25] op_sel_hi:[0,1]
	v_pk_mul_f32 v[20:21], v[32:33], v[20:21] op_sel_hi:[0,1]
	v_pk_fma_f32 v[14:15], v[14:15], s[38:39], v[150:151] op_sel_hi:[1,0,1]
	v_pk_fma_f32 v[6:7], v[10:11], s[38:39], v[6:7] op_sel_hi:[1,0,1]
	v_lshl_add_u64 v[46:47], v[46:47], 0, s[8:9]
	v_med3_f32 v24, v24, s75, v164
	v_med3_f32 v20, v20, s75, v164
	v_med3_f32 v1, v25, s75, v164
	v_med3_f32 v5, v21, s75, v164
	v_pk_mul_f32 v[14:15], v[32:33], v[14:15] op_sel_hi:[0,1]
	v_pk_mul_f32 v[6:7], v[32:33], v[6:7] op_sel_hi:[0,1]
	v_lshl_add_u64 v[28:29], v[46:47], 0, v[146:147]
	v_cvt_pk_fp8_f32 v18, v24, v1 op_sel:[0,0,1]
	v_cvt_pk_fp8_f32 v19, v20, v5 op_sel:[0,0,1]
	v_med3_f32 v1, v14, s75, v164
	v_med3_f32 v5, v6, s75, v164
	v_med3_f32 v10, v15, s75, v164
	v_med3_f32 v11, v7, s75, v164
	v_mov_b32_e32 v6, v147
	v_mov_b32_e32 v7, v147
	s_waitcnt lgkmcnt(0)
	global_store_dwordx4 v[28:29], v[42:45], off
	v_cvt_pk_fp8_f32 v6, v1, v10
	v_cvt_pk_fp8_f32 v7, v5, v11
	ds_write2_b64 v122, v[34:35], v[26:27] offset1:4
	v_add_u32_e32 v30, 0xa0, v4
	v_pk_fma_f32 v[8:9], v[16:17], s[38:39], v[8:9] op_sel_hi:[1,0,1]
	v_pk_fma_f32 v[2:3], v[12:13], s[38:39], v[2:3] op_sel_hi:[1,0,1]
	ds_read_b128 v[26:29], v123
	v_ashrrev_i32_e32 v31, 31, v30
	v_pk_mul_f32 v[8:9], v[32:33], v[8:9] op_sel_hi:[0,1]
	v_pk_mul_f32 v[2:3], v[32:33], v[2:3] op_sel_hi:[0,1]
	v_lshlrev_b64 v[30:31], 10, v[30:31]
	v_med3_f32 v8, v8, s75, v164
	v_med3_f32 v2, v2, s75, v164
	v_med3_f32 v1, v9, s75, v164
	v_med3_f32 v3, v3, s75, v164
	v_lshl_add_u64 v[30:31], s[16:17], 0, v[30:31]
	v_cvt_pk_fp8_f32 v6, v8, v1 op_sel:[0,0,1]
	v_cvt_pk_fp8_f32 v7, v2, v3 op_sel:[0,0,1]
	v_lshl_add_u64 v[30:31], v[30:31], 0, s[8:9]
	v_lshl_add_u64 v[2:3], v[30:31], 0, v[146:147]
	s_waitcnt lgkmcnt(0)
	global_store_dwordx4 v[2:3], v[26:29], off
	ds_write2_b64 v122, v[18:19], v[6:7] offset1:4
	v_add_u32_e32 v2, 0xb0, v4
	ds_read_b128 v[6:9], v123
	v_ashrrev_i32_e32 v3, 31, v2
	v_lshlrev_b64 v[2:3], 10, v[2:3]
	v_lshl_add_u64 v[2:3], s[16:17], 0, v[2:3]
	v_lshl_add_u64 v[2:3], v[2:3], 0, s[8:9]
	v_lshl_add_u64 v[2:3], v[2:3], 0, v[146:147]
	s_waitcnt lgkmcnt(0)
	global_store_dwordx4 v[2:3], v[6:9], off
	s_and_b64 vcc, exec, s[10:11]
	s_mov_b64 s[8:9], -1
	s_cbranch_vccnz .LBB0_3418
	v_mov_b32_e32 v12, v0
	s_lshl_b32 s9, s42, 8
	v_readfirstlane_b32 s8, v12
	s_and_b32 s10, s8, 0xc0
	s_ashr_i32 s8, s8, 2
	s_andn2_b32 s8, s8, 63
	s_add_i32 s8, s8, s9
	v_and_or_b32 v2, v12, 15, s8
	v_ashrrev_i32_e32 v3, 31, v2
	s_lshl_b64 s[8:9], s[44:45], 11
	v_lshl_add_u64 v[4:5], v[2:3], 2, s[12:13]
	v_add_u32_e32 v6, 0x80, v2
	v_add_u32_e32 v8, 0x90, v2
	v_add_u32_e32 v10, 0xa0, v2
	v_add_u32_e32 v2, 0xb0, v2
	s_add_u32 s11, s54, s8
	v_ashrrev_i32_e32 v7, 31, v6
	v_ashrrev_i32_e32 v9, 31, v8
	v_ashrrev_i32_e32 v11, 31, v10
	v_ashrrev_i32_e32 v3, 31, v2
	s_addc_u32 s41, s55, s9
	s_lshl_b32 s8, s40, 8
	v_lshl_add_u64 v[6:7], v[6:7], 2, s[12:13]
	v_lshl_add_u64 v[8:9], v[8:9], 2, s[12:13]
	v_lshl_add_u64 v[10:11], v[10:11], 2, s[12:13]
	v_lshl_add_u64 v[2:3], v[2:3], 2, s[12:13]
	global_load_dword v146, v[4:5], off
	global_load_dword v170, v[4:5], off offset:64
	global_load_dword v169, v[4:5], off offset:128
	global_load_dword v168, v[4:5], off offset:192
	global_load_dword v167, v[6:7], off
	global_load_dword v166, v[8:9], off
	global_load_dword v165, v[10:11], off
	global_load_dword v1, v[2:3], off
	s_ashr_i32 s9, s8, 31
	s_lshl_b64 s[8:9], s[8:9], 1
	s_add_u32 s8, s11, s8
	s_addc_u32 s9, s41, s9
	s_lshl_b32 s10, s10, 1
	s_add_u32 s8, s8, s10
	s_addc_u32 s9, s9, 0
	v_and_b32_e32 v2, 48, v12
	global_load_dwordx4 v[6:9], v2, s[8:9]
	s_nop 0
	global_load_dwordx4 v[2:5], v2, s[8:9] offset:64
	s_andn2_b64 vcc, exec, s[14:15]
	s_cbranch_vccnz .LBB0_3417
	s_barrier
	s_branch .LBB0_3417
